# s14
# speedup vs baseline: 1.0708x; 1.0083x over previous
.LBB0_3:
	s_cmpk_gt_u32 s10, 0x17f
	s_cbranch_scc0 .LBB0_7
	s_load_dwordx2 s[4:5], s[0:1], 0x0
	s_load_dwordx2 s[6:7], s[0:1], 0x18
	s_load_dwordx2 s[12:13], s[0:1], 0x20
	s_load_dwordx2 s[14:15], s[0:1], 0x38
	s_sub_i32 s8, s10, 0x180
	s_lshr_b32 s2, s8, 1
	s_and_b32 s3, s8, 1
	s_lshl_b32 s9, s2, 5
	s_lshl_b32 s11, s2, 15
	s_lshl_b32 s3, s3, 16
	v_and_b32_e32 v1, 63, v0
	v_lshrrev_b32_e32 v2, 6, v0
	v_lshlrev_b32_e32 v1, 6, v1
	v_add_u32_e32 v4, s11, v1
	v_lshl_add_u32 v3, v2, 14, v1
	v_add_u32_e32 v3, s3, v3
	v_lshlrev_b32_e32 v10, 14, v2
	v_add_u32_e32 v10, s3, v10
	s_waitcnt lgkmcnt(0)
	s_load_dwordx8 s[16:23], s[12:13], s9
	v_add_u32_e32 v10, s9, v10
	global_load_dwordx4 v[12:15], v4, s[6:7]
	global_load_dwordx4 v[16:19], v4, s[6:7] offset:16
	global_load_dwordx4 v[20:23], v4, s[6:7] offset:32
	global_load_dwordx4 v[24:27], v4, s[6:7] offset:48
	v_add_u32_e32 v6, 0x1000, v4
	global_load_dwordx4 v[28:31], v6, s[6:7]
	global_load_dwordx4 v[32:35], v6, s[6:7] offset:16
	global_load_dwordx4 v[36:39], v6, s[6:7] offset:32
	global_load_dwordx4 v[40:43], v6, s[6:7] offset:48
	v_add_u32_e32 v5, 0x2000, v4
	global_load_dwordx4 v[44:47], v5, s[6:7]
	global_load_dwordx4 v[48:51], v5, s[6:7] offset:16
	global_load_dwordx4 v[52:55], v5, s[6:7] offset:32
	global_load_dwordx4 v[56:59], v5, s[6:7] offset:48
	v_add_u32_e32 v6, 0x3000, v4
	global_load_dwordx4 v[60:63], v6, s[6:7]
	global_load_dwordx4 v[64:67], v6, s[6:7] offset:16
	global_load_dwordx4 v[68:71], v6, s[6:7] offset:32
	global_load_dwordx4 v[72:75], v6, s[6:7] offset:48
	v_add_u32_e32 v5, 0x4000, v4
	global_load_dwordx4 v[76:79], v5, s[6:7]
	global_load_dwordx4 v[80:83], v5, s[6:7] offset:16
	global_load_dwordx4 v[84:87], v5, s[6:7] offset:32
	global_load_dwordx4 v[88:91], v5, s[6:7] offset:48
	v_add_u32_e32 v6, 0x5000, v4
	global_load_dwordx4 v[92:95], v6, s[6:7]
	global_load_dwordx4 v[96:99], v6, s[6:7] offset:16
	global_load_dwordx4 v[100:103], v6, s[6:7] offset:32
	global_load_dwordx4 v[104:107], v6, s[6:7] offset:48
	v_add_u32_e32 v5, 0x6000, v4
	global_load_dwordx4 v[108:111], v5, s[6:7]
	global_load_dwordx4 v[112:115], v5, s[6:7] offset:16
	global_load_dwordx4 v[116:119], v5, s[6:7] offset:32
	global_load_dwordx4 v[120:123], v5, s[6:7] offset:48
	v_add_u32_e32 v6, 0x7000, v4
	global_load_dwordx4 v[124:127], v6, s[6:7]
	global_load_dwordx4 v[128:131], v6, s[6:7] offset:16
	global_load_dwordx4 v[132:135], v6, s[6:7] offset:32
	global_load_dwordx4 v[136:139], v6, s[6:7] offset:48
	global_load_dwordx4 v[140:143], v3, s[4:5]
	global_load_dwordx4 v[144:147], v3, s[4:5] offset:16
	global_load_dwordx4 v[148:151], v3, s[4:5] offset:32
	global_load_dwordx4 v[152:155], v3, s[4:5] offset:48
	v_add_u32_e32 v9, 0x1000, v3
	global_load_dwordx4 v[156:159], v9, s[4:5]
	global_load_dwordx4 v[160:163], v9, s[4:5] offset:16
	global_load_dwordx4 v[164:167], v9, s[4:5] offset:32
	global_load_dwordx4 v[168:171], v9, s[4:5] offset:48
	v_add_u32_e32 v8, 0x2000, v3
	global_load_dwordx4 v[172:175], v8, s[4:5]
	global_load_dwordx4 v[176:179], v8, s[4:5] offset:16
	global_load_dwordx4 v[180:183], v8, s[4:5] offset:32
	global_load_dwordx4 v[184:187], v8, s[4:5] offset:48
	v_add_u32_e32 v9, 0x3000, v3
	global_load_dwordx4 v[188:191], v9, s[4:5]
	global_load_dwordx4 v[192:195], v9, s[4:5] offset:16
	global_load_dwordx4 v[196:199], v9, s[4:5] offset:32
	global_load_dwordx4 v[200:203], v9, s[4:5] offset:48
	s_waitcnt vmcnt(12)
	v_mul_f32_e32 v204, v12, v140
	v_mul_f32_e32 v205, v28, v140
	v_mul_f32_e32 v206, v44, v140
	v_mul_f32_e32 v207, v60, v140
	v_mul_f32_e32 v208, v76, v140
	v_mul_f32_e32 v209, v92, v140
	v_mul_f32_e32 v210, v108, v140
	v_mul_f32_e32 v211, v124, v140
	v_fmac_f32_e32 v204, v13, v141
	v_fmac_f32_e32 v205, v29, v141
	v_fmac_f32_e32 v206, v45, v141
	v_fmac_f32_e32 v207, v61, v141
	v_fmac_f32_e32 v208, v77, v141
	v_fmac_f32_e32 v209, v93, v141
	v_fmac_f32_e32 v210, v109, v141
	v_fmac_f32_e32 v211, v125, v141
	v_fmac_f32_e32 v204, v14, v142
	v_fmac_f32_e32 v205, v30, v142
	v_fmac_f32_e32 v206, v46, v142
	v_fmac_f32_e32 v207, v62, v142
	v_fmac_f32_e32 v208, v78, v142
	v_fmac_f32_e32 v209, v94, v142
	v_fmac_f32_e32 v210, v110, v142
	v_fmac_f32_e32 v211, v126, v142
	v_fmac_f32_e32 v204, v15, v143
	v_fmac_f32_e32 v205, v31, v143
	v_fmac_f32_e32 v206, v47, v143
	v_fmac_f32_e32 v207, v63, v143
	v_fmac_f32_e32 v208, v79, v143
	v_fmac_f32_e32 v209, v95, v143
	v_fmac_f32_e32 v210, v111, v143
	v_fmac_f32_e32 v211, v127, v143
	v_fmac_f32_e32 v204, v16, v144
	v_fmac_f32_e32 v205, v32, v144
	v_fmac_f32_e32 v206, v48, v144
	v_fmac_f32_e32 v207, v64, v144
	v_fmac_f32_e32 v208, v80, v144
	v_fmac_f32_e32 v209, v96, v144
	v_fmac_f32_e32 v210, v112, v144
	v_fmac_f32_e32 v211, v128, v144
	v_fmac_f32_e32 v204, v17, v145
	v_fmac_f32_e32 v205, v33, v145
	v_fmac_f32_e32 v206, v49, v145
	v_fmac_f32_e32 v207, v65, v145
	v_fmac_f32_e32 v208, v81, v145
	v_fmac_f32_e32 v209, v97, v145
	v_fmac_f32_e32 v210, v113, v145
	v_fmac_f32_e32 v211, v129, v145
	v_fmac_f32_e32 v204, v18, v146
	v_fmac_f32_e32 v205, v34, v146
	v_fmac_f32_e32 v206, v50, v146
	v_fmac_f32_e32 v207, v66, v146
	v_fmac_f32_e32 v208, v82, v146
	v_fmac_f32_e32 v209, v98, v146
	v_fmac_f32_e32 v210, v114, v146
	v_fmac_f32_e32 v211, v130, v146
	v_fmac_f32_e32 v204, v19, v147
	v_fmac_f32_e32 v205, v35, v147
	v_fmac_f32_e32 v206, v51, v147
	v_fmac_f32_e32 v207, v67, v147
	v_fmac_f32_e32 v208, v83, v147
	v_fmac_f32_e32 v209, v99, v147
	v_fmac_f32_e32 v210, v115, v147
	v_fmac_f32_e32 v211, v131, v147
	v_fmac_f32_e32 v204, v20, v148
	v_fmac_f32_e32 v205, v36, v148
	v_fmac_f32_e32 v206, v52, v148
	v_fmac_f32_e32 v207, v68, v148
	v_fmac_f32_e32 v208, v84, v148
	v_fmac_f32_e32 v209, v100, v148
	v_fmac_f32_e32 v210, v116, v148
	v_fmac_f32_e32 v211, v132, v148
	v_fmac_f32_e32 v204, v21, v149
	v_fmac_f32_e32 v205, v37, v149
	v_fmac_f32_e32 v206, v53, v149
	v_fmac_f32_e32 v207, v69, v149
	v_fmac_f32_e32 v208, v85, v149
	v_fmac_f32_e32 v209, v101, v149
	v_fmac_f32_e32 v210, v117, v149
	v_fmac_f32_e32 v211, v133, v149
	v_fmac_f32_e32 v204, v22, v150
	v_fmac_f32_e32 v205, v38, v150
	v_fmac_f32_e32 v206, v54, v150
	v_fmac_f32_e32 v207, v70, v150
	v_fmac_f32_e32 v208, v86, v150
	v_fmac_f32_e32 v209, v102, v150
	v_fmac_f32_e32 v210, v118, v150
	v_fmac_f32_e32 v211, v134, v150
	v_fmac_f32_e32 v204, v23, v151
	v_fmac_f32_e32 v205, v39, v151
	v_fmac_f32_e32 v206, v55, v151
	v_fmac_f32_e32 v207, v71, v151
	v_fmac_f32_e32 v208, v87, v151
	v_fmac_f32_e32 v209, v103, v151
	v_fmac_f32_e32 v210, v119, v151
	v_fmac_f32_e32 v211, v135, v151
	v_fmac_f32_e32 v204, v24, v152
	v_fmac_f32_e32 v205, v40, v152
	v_fmac_f32_e32 v206, v56, v152
	v_fmac_f32_e32 v207, v72, v152
	v_fmac_f32_e32 v208, v88, v152
	v_fmac_f32_e32 v209, v104, v152
	v_fmac_f32_e32 v210, v120, v152
	v_fmac_f32_e32 v211, v136, v152
	v_fmac_f32_e32 v204, v25, v153
	v_fmac_f32_e32 v205, v41, v153
	v_fmac_f32_e32 v206, v57, v153
	v_fmac_f32_e32 v207, v73, v153
	v_fmac_f32_e32 v208, v89, v153
	v_fmac_f32_e32 v209, v105, v153
	v_fmac_f32_e32 v210, v121, v153
	v_fmac_f32_e32 v211, v137, v153
	v_fmac_f32_e32 v204, v26, v154
	v_fmac_f32_e32 v205, v42, v154
	v_fmac_f32_e32 v206, v58, v154
	v_fmac_f32_e32 v207, v74, v154
	v_fmac_f32_e32 v208, v90, v154
	v_fmac_f32_e32 v209, v106, v154
	v_fmac_f32_e32 v210, v122, v154
	v_fmac_f32_e32 v211, v138, v154
	v_fmac_f32_e32 v204, v27, v155
	v_fmac_f32_e32 v205, v43, v155
	v_fmac_f32_e32 v206, v59, v155
	v_fmac_f32_e32 v207, v75, v155
	v_fmac_f32_e32 v208, v91, v155
	v_fmac_f32_e32 v209, v107, v155
	v_fmac_f32_e32 v210, v123, v155
	v_fmac_f32_e32 v211, v139, v155
	s_waitcnt vmcnt(8)
	v_mul_f32_e32 v212, v12, v156
	v_mul_f32_e32 v213, v28, v156
	v_mul_f32_e32 v214, v44, v156
	v_mul_f32_e32 v215, v60, v156
	v_mul_f32_e32 v216, v76, v156
	v_mul_f32_e32 v217, v92, v156
	v_mul_f32_e32 v218, v108, v156
	v_mul_f32_e32 v219, v124, v156
	v_fmac_f32_e32 v212, v13, v157
	v_fmac_f32_e32 v213, v29, v157
	v_fmac_f32_e32 v214, v45, v157
	v_fmac_f32_e32 v215, v61, v157
	v_fmac_f32_e32 v216, v77, v157
	v_fmac_f32_e32 v217, v93, v157
	v_fmac_f32_e32 v218, v109, v157
	v_fmac_f32_e32 v219, v125, v157
	v_fmac_f32_e32 v212, v14, v158
	v_fmac_f32_e32 v213, v30, v158
	v_fmac_f32_e32 v214, v46, v158
	v_fmac_f32_e32 v215, v62, v158
	v_fmac_f32_e32 v216, v78, v158
	v_fmac_f32_e32 v217, v94, v158
	v_fmac_f32_e32 v218, v110, v158
	v_fmac_f32_e32 v219, v126, v158
	v_fmac_f32_e32 v212, v15, v159
	v_fmac_f32_e32 v213, v31, v159
	v_fmac_f32_e32 v214, v47, v159
	v_fmac_f32_e32 v215, v63, v159
	v_fmac_f32_e32 v216, v79, v159
	v_fmac_f32_e32 v217, v95, v159
	v_fmac_f32_e32 v218, v111, v159
	v_fmac_f32_e32 v219, v127, v159
	v_fmac_f32_e32 v212, v16, v160
	v_fmac_f32_e32 v213, v32, v160
	v_fmac_f32_e32 v214, v48, v160
	v_fmac_f32_e32 v215, v64, v160
	v_fmac_f32_e32 v216, v80, v160
	v_fmac_f32_e32 v217, v96, v160
	v_fmac_f32_e32 v218, v112, v160
	v_fmac_f32_e32 v219, v128, v160
	v_fmac_f32_e32 v212, v17, v161
	v_fmac_f32_e32 v213, v33, v161
	v_fmac_f32_e32 v214, v49, v161
	v_fmac_f32_e32 v215, v65, v161
	v_fmac_f32_e32 v216, v81, v161
	v_fmac_f32_e32 v217, v97, v161
	v_fmac_f32_e32 v218, v113, v161
	v_fmac_f32_e32 v219, v129, v161
	v_fmac_f32_e32 v212, v18, v162
	v_fmac_f32_e32 v213, v34, v162
	v_fmac_f32_e32 v214, v50, v162
	v_fmac_f32_e32 v215, v66, v162
	v_fmac_f32_e32 v216, v82, v162
	v_fmac_f32_e32 v217, v98, v162
	v_fmac_f32_e32 v218, v114, v162
	v_fmac_f32_e32 v219, v130, v162
	v_fmac_f32_e32 v212, v19, v163
	v_fmac_f32_e32 v213, v35, v163
	v_fmac_f32_e32 v214, v51, v163
	v_fmac_f32_e32 v215, v67, v163
	v_fmac_f32_e32 v216, v83, v163
	v_fmac_f32_e32 v217, v99, v163
	v_fmac_f32_e32 v218, v115, v163
	v_fmac_f32_e32 v219, v131, v163
	v_fmac_f32_e32 v212, v20, v164
	v_fmac_f32_e32 v213, v36, v164
	v_fmac_f32_e32 v214, v52, v164
	v_fmac_f32_e32 v215, v68, v164
	v_fmac_f32_e32 v216, v84, v164
	v_fmac_f32_e32 v217, v100, v164
	v_fmac_f32_e32 v218, v116, v164
	v_fmac_f32_e32 v219, v132, v164
	v_fmac_f32_e32 v212, v21, v165
	v_fmac_f32_e32 v213, v37, v165
	v_fmac_f32_e32 v214, v53, v165
	v_fmac_f32_e32 v215, v69, v165
	v_fmac_f32_e32 v216, v85, v165
	v_fmac_f32_e32 v217, v101, v165
	v_fmac_f32_e32 v218, v117, v165
	v_fmac_f32_e32 v219, v133, v165
	v_fmac_f32_e32 v212, v22, v166
	v_fmac_f32_e32 v213, v38, v166
	v_fmac_f32_e32 v214, v54, v166
	v_fmac_f32_e32 v215, v70, v166
	v_fmac_f32_e32 v216, v86, v166
	v_fmac_f32_e32 v217, v102, v166
	v_fmac_f32_e32 v218, v118, v166
	v_fmac_f32_e32 v219, v134, v166
	v_fmac_f32_e32 v212, v23, v167
	v_fmac_f32_e32 v213, v39, v167
	v_fmac_f32_e32 v214, v55, v167
	v_fmac_f32_e32 v215, v71, v167
	v_fmac_f32_e32 v216, v87, v167
	v_fmac_f32_e32 v217, v103, v167
	v_fmac_f32_e32 v218, v119, v167
	v_fmac_f32_e32 v219, v135, v167
	v_fmac_f32_e32 v212, v24, v168
	v_fmac_f32_e32 v213, v40, v168
	v_fmac_f32_e32 v214, v56, v168
	v_fmac_f32_e32 v215, v72, v168
	v_fmac_f32_e32 v216, v88, v168
	v_fmac_f32_e32 v217, v104, v168
	v_fmac_f32_e32 v218, v120, v168
	v_fmac_f32_e32 v219, v136, v168
	v_fmac_f32_e32 v212, v25, v169
	v_fmac_f32_e32 v213, v41, v169
	v_fmac_f32_e32 v214, v57, v169
	v_fmac_f32_e32 v215, v73, v169
	v_fmac_f32_e32 v216, v89, v169
	v_fmac_f32_e32 v217, v105, v169
	v_fmac_f32_e32 v218, v121, v169
	v_fmac_f32_e32 v219, v137, v169
	v_fmac_f32_e32 v212, v26, v170
	v_fmac_f32_e32 v213, v42, v170
	v_fmac_f32_e32 v214, v58, v170
	v_fmac_f32_e32 v215, v74, v170
	v_fmac_f32_e32 v216, v90, v170
	v_fmac_f32_e32 v217, v106, v170
	v_fmac_f32_e32 v218, v122, v170
	v_fmac_f32_e32 v219, v138, v170
	v_fmac_f32_e32 v212, v27, v171
	v_fmac_f32_e32 v213, v43, v171
	v_fmac_f32_e32 v214, v59, v171
	v_fmac_f32_e32 v215, v75, v171
	v_fmac_f32_e32 v216, v91, v171
	v_fmac_f32_e32 v217, v107, v171
	v_fmac_f32_e32 v218, v123, v171
	v_fmac_f32_e32 v219, v139, v171
	s_waitcnt vmcnt(4)
	v_mul_f32_e32 v220, v12, v172
	v_mul_f32_e32 v221, v28, v172
	v_mul_f32_e32 v222, v44, v172
	v_mul_f32_e32 v223, v60, v172
	v_mul_f32_e32 v224, v76, v172
	v_mul_f32_e32 v225, v92, v172
	v_mul_f32_e32 v226, v108, v172
	v_mul_f32_e32 v227, v124, v172
	v_fmac_f32_e32 v220, v13, v173
	v_fmac_f32_e32 v221, v29, v173
	v_fmac_f32_e32 v222, v45, v173
	v_fmac_f32_e32 v223, v61, v173
	v_fmac_f32_e32 v224, v77, v173
	v_fmac_f32_e32 v225, v93, v173
	v_fmac_f32_e32 v226, v109, v173
	v_fmac_f32_e32 v227, v125, v173
	v_fmac_f32_e32 v220, v14, v174
	v_fmac_f32_e32 v221, v30, v174
	v_fmac_f32_e32 v222, v46, v174
	v_fmac_f32_e32 v223, v62, v174
	v_fmac_f32_e32 v224, v78, v174
	v_fmac_f32_e32 v225, v94, v174
	v_fmac_f32_e32 v226, v110, v174
	v_fmac_f32_e32 v227, v126, v174
	v_fmac_f32_e32 v220, v15, v175
	v_fmac_f32_e32 v221, v31, v175
	v_fmac_f32_e32 v222, v47, v175
	v_fmac_f32_e32 v223, v63, v175
	v_fmac_f32_e32 v224, v79, v175
	v_fmac_f32_e32 v225, v95, v175
	v_fmac_f32_e32 v226, v111, v175
	v_fmac_f32_e32 v227, v127, v175
	v_fmac_f32_e32 v220, v16, v176
	v_fmac_f32_e32 v221, v32, v176
	v_fmac_f32_e32 v222, v48, v176
	v_fmac_f32_e32 v223, v64, v176
	v_fmac_f32_e32 v224, v80, v176
	v_fmac_f32_e32 v225, v96, v176
	v_fmac_f32_e32 v226, v112, v176
	v_fmac_f32_e32 v227, v128, v176
	v_fmac_f32_e32 v220, v17, v177
	v_fmac_f32_e32 v221, v33, v177
	v_fmac_f32_e32 v222, v49, v177
	v_fmac_f32_e32 v223, v65, v177
	v_fmac_f32_e32 v224, v81, v177
	v_fmac_f32_e32 v225, v97, v177
	v_fmac_f32_e32 v226, v113, v177
	v_fmac_f32_e32 v227, v129, v177
	v_fmac_f32_e32 v220, v18, v178
	v_fmac_f32_e32 v221, v34, v178
	v_fmac_f32_e32 v222, v50, v178
	v_fmac_f32_e32 v223, v66, v178
	v_fmac_f32_e32 v224, v82, v178
	v_fmac_f32_e32 v225, v98, v178
	v_fmac_f32_e32 v226, v114, v178
	v_fmac_f32_e32 v227, v130, v178
	v_fmac_f32_e32 v220, v19, v179
	v_fmac_f32_e32 v221, v35, v179
	v_fmac_f32_e32 v222, v51, v179
	v_fmac_f32_e32 v223, v67, v179
	v_fmac_f32_e32 v224, v83, v179
	v_fmac_f32_e32 v225, v99, v179
	v_fmac_f32_e32 v226, v115, v179
	v_fmac_f32_e32 v227, v131, v179
	v_fmac_f32_e32 v220, v20, v180
	v_fmac_f32_e32 v221, v36, v180
	v_fmac_f32_e32 v222, v52, v180
	v_fmac_f32_e32 v223, v68, v180
	v_fmac_f32_e32 v224, v84, v180
	v_fmac_f32_e32 v225, v100, v180
	v_fmac_f32_e32 v226, v116, v180
	v_fmac_f32_e32 v227, v132, v180
	v_fmac_f32_e32 v220, v21, v181
	v_fmac_f32_e32 v221, v37, v181
	v_fmac_f32_e32 v222, v53, v181
	v_fmac_f32_e32 v223, v69, v181
	v_fmac_f32_e32 v224, v85, v181
	v_fmac_f32_e32 v225, v101, v181
	v_fmac_f32_e32 v226, v117, v181
	v_fmac_f32_e32 v227, v133, v181
	v_fmac_f32_e32 v220, v22, v182
	v_fmac_f32_e32 v221, v38, v182
	v_fmac_f32_e32 v222, v54, v182
	v_fmac_f32_e32 v223, v70, v182
	v_fmac_f32_e32 v224, v86, v182
	v_fmac_f32_e32 v225, v102, v182
	v_fmac_f32_e32 v226, v118, v182
	v_fmac_f32_e32 v227, v134, v182
	v_fmac_f32_e32 v220, v23, v183
	v_fmac_f32_e32 v221, v39, v183
	v_fmac_f32_e32 v222, v55, v183
	v_fmac_f32_e32 v223, v71, v183
	v_fmac_f32_e32 v224, v87, v183
	v_fmac_f32_e32 v225, v103, v183
	v_fmac_f32_e32 v226, v119, v183
	v_fmac_f32_e32 v227, v135, v183
	v_fmac_f32_e32 v220, v24, v184
	v_fmac_f32_e32 v221, v40, v184
	v_fmac_f32_e32 v222, v56, v184
	v_fmac_f32_e32 v223, v72, v184
	v_fmac_f32_e32 v224, v88, v184
	v_fmac_f32_e32 v225, v104, v184
	v_fmac_f32_e32 v226, v120, v184
	v_fmac_f32_e32 v227, v136, v184
	v_fmac_f32_e32 v220, v25, v185
	v_fmac_f32_e32 v221, v41, v185
	v_fmac_f32_e32 v222, v57, v185
	v_fmac_f32_e32 v223, v73, v185
	v_fmac_f32_e32 v224, v89, v185
	v_fmac_f32_e32 v225, v105, v185
	v_fmac_f32_e32 v226, v121, v185
	v_fmac_f32_e32 v227, v137, v185
	v_fmac_f32_e32 v220, v26, v186
	v_fmac_f32_e32 v221, v42, v186
	v_fmac_f32_e32 v222, v58, v186
	v_fmac_f32_e32 v223, v74, v186
	v_fmac_f32_e32 v224, v90, v186
	v_fmac_f32_e32 v225, v106, v186
	v_fmac_f32_e32 v226, v122, v186
	v_fmac_f32_e32 v227, v138, v186
	v_fmac_f32_e32 v220, v27, v187
	v_fmac_f32_e32 v221, v43, v187
	v_fmac_f32_e32 v222, v59, v187
	v_fmac_f32_e32 v223, v75, v187
	v_fmac_f32_e32 v224, v91, v187
	v_fmac_f32_e32 v225, v107, v187
	v_fmac_f32_e32 v226, v123, v187
	v_fmac_f32_e32 v227, v139, v187
	s_waitcnt vmcnt(0)
	v_mul_f32_e32 v228, v12, v188
	v_mul_f32_e32 v229, v28, v188
	v_mul_f32_e32 v230, v44, v188
	v_mul_f32_e32 v231, v60, v188
	v_mul_f32_e32 v232, v76, v188
	v_mul_f32_e32 v233, v92, v188
	v_mul_f32_e32 v234, v108, v188
	v_mul_f32_e32 v235, v124, v188
	v_fmac_f32_e32 v228, v13, v189
	v_fmac_f32_e32 v229, v29, v189
	v_fmac_f32_e32 v230, v45, v189
	v_fmac_f32_e32 v231, v61, v189
	v_fmac_f32_e32 v232, v77, v189
	v_fmac_f32_e32 v233, v93, v189
	v_fmac_f32_e32 v234, v109, v189
	v_fmac_f32_e32 v235, v125, v189
	v_fmac_f32_e32 v228, v14, v190
	v_fmac_f32_e32 v229, v30, v190
	v_fmac_f32_e32 v230, v46, v190
	v_fmac_f32_e32 v231, v62, v190
	v_fmac_f32_e32 v232, v78, v190
	v_fmac_f32_e32 v233, v94, v190
	v_fmac_f32_e32 v234, v110, v190
	v_fmac_f32_e32 v235, v126, v190
	v_fmac_f32_e32 v228, v15, v191
	v_fmac_f32_e32 v229, v31, v191
	v_fmac_f32_e32 v230, v47, v191
	v_fmac_f32_e32 v231, v63, v191
	v_fmac_f32_e32 v232, v79, v191
	v_fmac_f32_e32 v233, v95, v191
	v_fmac_f32_e32 v234, v111, v191
	v_fmac_f32_e32 v235, v127, v191
	v_fmac_f32_e32 v228, v16, v192
	v_fmac_f32_e32 v229, v32, v192
	v_fmac_f32_e32 v230, v48, v192
	v_fmac_f32_e32 v231, v64, v192
	v_fmac_f32_e32 v232, v80, v192
	v_fmac_f32_e32 v233, v96, v192
	v_fmac_f32_e32 v234, v112, v192
	v_fmac_f32_e32 v235, v128, v192
	v_fmac_f32_e32 v228, v17, v193
	v_fmac_f32_e32 v229, v33, v193
	v_fmac_f32_e32 v230, v49, v193
	v_fmac_f32_e32 v231, v65, v193
	v_fmac_f32_e32 v232, v81, v193
	v_fmac_f32_e32 v233, v97, v193
	v_fmac_f32_e32 v234, v113, v193
	v_fmac_f32_e32 v235, v129, v193
	v_fmac_f32_e32 v228, v18, v194
	v_fmac_f32_e32 v229, v34, v194
	v_fmac_f32_e32 v230, v50, v194
	v_fmac_f32_e32 v231, v66, v194
	v_fmac_f32_e32 v232, v82, v194
	v_fmac_f32_e32 v233, v98, v194
	v_fmac_f32_e32 v234, v114, v194
	v_fmac_f32_e32 v235, v130, v194
	v_fmac_f32_e32 v228, v19, v195
	v_fmac_f32_e32 v229, v35, v195
	v_fmac_f32_e32 v230, v51, v195
	v_fmac_f32_e32 v231, v67, v195
	v_fmac_f32_e32 v232, v83, v195
	v_fmac_f32_e32 v233, v99, v195
	v_fmac_f32_e32 v234, v115, v195
	v_fmac_f32_e32 v235, v131, v195
	v_fmac_f32_e32 v228, v20, v196
	v_fmac_f32_e32 v229, v36, v196
	v_fmac_f32_e32 v230, v52, v196
	v_fmac_f32_e32 v231, v68, v196
	v_fmac_f32_e32 v232, v84, v196
	v_fmac_f32_e32 v233, v100, v196
	v_fmac_f32_e32 v234, v116, v196
	v_fmac_f32_e32 v235, v132, v196
	v_fmac_f32_e32 v228, v21, v197
	v_fmac_f32_e32 v229, v37, v197
	v_fmac_f32_e32 v230, v53, v197
	v_fmac_f32_e32 v231, v69, v197
	v_fmac_f32_e32 v232, v85, v197
	v_fmac_f32_e32 v233, v101, v197
	v_fmac_f32_e32 v234, v117, v197
	v_fmac_f32_e32 v235, v133, v197
	v_fmac_f32_e32 v228, v22, v198
	v_fmac_f32_e32 v229, v38, v198
	v_fmac_f32_e32 v230, v54, v198
	v_fmac_f32_e32 v231, v70, v198
	v_fmac_f32_e32 v232, v86, v198
	v_fmac_f32_e32 v233, v102, v198
	v_fmac_f32_e32 v234, v118, v198
	v_fmac_f32_e32 v235, v134, v198
	v_fmac_f32_e32 v228, v23, v199
	v_fmac_f32_e32 v229, v39, v199
	v_fmac_f32_e32 v230, v55, v199
	v_fmac_f32_e32 v231, v71, v199
	v_fmac_f32_e32 v232, v87, v199
	v_fmac_f32_e32 v233, v103, v199
	v_fmac_f32_e32 v234, v119, v199
	v_fmac_f32_e32 v235, v135, v199
	v_fmac_f32_e32 v228, v24, v200
	v_fmac_f32_e32 v229, v40, v200
	v_fmac_f32_e32 v230, v56, v200
	v_fmac_f32_e32 v231, v72, v200
	v_fmac_f32_e32 v232, v88, v200
	v_fmac_f32_e32 v233, v104, v200
	v_fmac_f32_e32 v234, v120, v200
	v_fmac_f32_e32 v235, v136, v200
	v_fmac_f32_e32 v228, v25, v201
	v_fmac_f32_e32 v229, v41, v201
	v_fmac_f32_e32 v230, v57, v201
	v_fmac_f32_e32 v231, v73, v201
	v_fmac_f32_e32 v232, v89, v201
	v_fmac_f32_e32 v233, v105, v201
	v_fmac_f32_e32 v234, v121, v201
	v_fmac_f32_e32 v235, v137, v201
	v_fmac_f32_e32 v228, v26, v202
	v_fmac_f32_e32 v229, v42, v202
	v_fmac_f32_e32 v230, v58, v202
	v_fmac_f32_e32 v231, v74, v202
	v_fmac_f32_e32 v232, v90, v202
	v_fmac_f32_e32 v233, v106, v202
	v_fmac_f32_e32 v234, v122, v202
	v_fmac_f32_e32 v235, v138, v202
	v_fmac_f32_e32 v228, v27, v203
	v_fmac_f32_e32 v229, v43, v203
	v_fmac_f32_e32 v230, v59, v203
	v_fmac_f32_e32 v231, v75, v203
	v_fmac_f32_e32 v232, v91, v203
	v_fmac_f32_e32 v233, v107, v203
	v_fmac_f32_e32 v234, v123, v203
	v_fmac_f32_e32 v235, v139, v203
	s_nop 1
	v_add_f32_dpp v204, v204, v204 quad_perm:[1,0,3,2] row_mask:0xf bank_mask:0xf
	v_add_f32_dpp v205, v205, v205 quad_perm:[1,0,3,2] row_mask:0xf bank_mask:0xf
	v_add_f32_dpp v206, v206, v206 quad_perm:[1,0,3,2] row_mask:0xf bank_mask:0xf
	v_add_f32_dpp v207, v207, v207 quad_perm:[1,0,3,2] row_mask:0xf bank_mask:0xf
	v_add_f32_dpp v208, v208, v208 quad_perm:[1,0,3,2] row_mask:0xf bank_mask:0xf
	v_add_f32_dpp v209, v209, v209 quad_perm:[1,0,3,2] row_mask:0xf bank_mask:0xf
	v_add_f32_dpp v210, v210, v210 quad_perm:[1,0,3,2] row_mask:0xf bank_mask:0xf
	v_add_f32_dpp v211, v211, v211 quad_perm:[1,0,3,2] row_mask:0xf bank_mask:0xf
	v_add_f32_dpp v212, v212, v212 quad_perm:[1,0,3,2] row_mask:0xf bank_mask:0xf
	v_add_f32_dpp v213, v213, v213 quad_perm:[1,0,3,2] row_mask:0xf bank_mask:0xf
	v_add_f32_dpp v214, v214, v214 quad_perm:[1,0,3,2] row_mask:0xf bank_mask:0xf
	v_add_f32_dpp v215, v215, v215 quad_perm:[1,0,3,2] row_mask:0xf bank_mask:0xf
	v_add_f32_dpp v216, v216, v216 quad_perm:[1,0,3,2] row_mask:0xf bank_mask:0xf
	v_add_f32_dpp v217, v217, v217 quad_perm:[1,0,3,2] row_mask:0xf bank_mask:0xf
	v_add_f32_dpp v218, v218, v218 quad_perm:[1,0,3,2] row_mask:0xf bank_mask:0xf
	v_add_f32_dpp v219, v219, v219 quad_perm:[1,0,3,2] row_mask:0xf bank_mask:0xf
	v_add_f32_dpp v220, v220, v220 quad_perm:[1,0,3,2] row_mask:0xf bank_mask:0xf
	v_add_f32_dpp v221, v221, v221 quad_perm:[1,0,3,2] row_mask:0xf bank_mask:0xf
	v_add_f32_dpp v222, v222, v222 quad_perm:[1,0,3,2] row_mask:0xf bank_mask:0xf
	v_add_f32_dpp v223, v223, v223 quad_perm:[1,0,3,2] row_mask:0xf bank_mask:0xf
	v_add_f32_dpp v224, v224, v224 quad_perm:[1,0,3,2] row_mask:0xf bank_mask:0xf
	v_add_f32_dpp v225, v225, v225 quad_perm:[1,0,3,2] row_mask:0xf bank_mask:0xf
	v_add_f32_dpp v226, v226, v226 quad_perm:[1,0,3,2] row_mask:0xf bank_mask:0xf
	v_add_f32_dpp v227, v227, v227 quad_perm:[1,0,3,2] row_mask:0xf bank_mask:0xf
	v_add_f32_dpp v228, v228, v228 quad_perm:[1,0,3,2] row_mask:0xf bank_mask:0xf
	v_add_f32_dpp v229, v229, v229 quad_perm:[1,0,3,2] row_mask:0xf bank_mask:0xf
	v_add_f32_dpp v230, v230, v230 quad_perm:[1,0,3,2] row_mask:0xf bank_mask:0xf
	v_add_f32_dpp v231, v231, v231 quad_perm:[1,0,3,2] row_mask:0xf bank_mask:0xf
	v_add_f32_dpp v232, v232, v232 quad_perm:[1,0,3,2] row_mask:0xf bank_mask:0xf
	v_add_f32_dpp v233, v233, v233 quad_perm:[1,0,3,2] row_mask:0xf bank_mask:0xf
	v_add_f32_dpp v234, v234, v234 quad_perm:[1,0,3,2] row_mask:0xf bank_mask:0xf
	v_add_f32_dpp v235, v235, v235 quad_perm:[1,0,3,2] row_mask:0xf bank_mask:0xf
	v_add_f32_dpp v204, v204, v204 quad_perm:[2,3,0,1] row_mask:0xf bank_mask:0xf
	v_add_f32_dpp v205, v205, v205 quad_perm:[2,3,0,1] row_mask:0xf bank_mask:0xf
	v_add_f32_dpp v206, v206, v206 quad_perm:[2,3,0,1] row_mask:0xf bank_mask:0xf
	v_add_f32_dpp v207, v207, v207 quad_perm:[2,3,0,1] row_mask:0xf bank_mask:0xf
	v_add_f32_dpp v208, v208, v208 quad_perm:[2,3,0,1] row_mask:0xf bank_mask:0xf
	v_add_f32_dpp v209, v209, v209 quad_perm:[2,3,0,1] row_mask:0xf bank_mask:0xf
	v_add_f32_dpp v210, v210, v210 quad_perm:[2,3,0,1] row_mask:0xf bank_mask:0xf
	v_add_f32_dpp v211, v211, v211 quad_perm:[2,3,0,1] row_mask:0xf bank_mask:0xf
	v_add_f32_dpp v212, v212, v212 quad_perm:[2,3,0,1] row_mask:0xf bank_mask:0xf
	v_add_f32_dpp v213, v213, v213 quad_perm:[2,3,0,1] row_mask:0xf bank_mask:0xf
	v_add_f32_dpp v214, v214, v214 quad_perm:[2,3,0,1] row_mask:0xf bank_mask:0xf
	v_add_f32_dpp v215, v215, v215 quad_perm:[2,3,0,1] row_mask:0xf bank_mask:0xf
	v_add_f32_dpp v216, v216, v216 quad_perm:[2,3,0,1] row_mask:0xf bank_mask:0xf
	v_add_f32_dpp v217, v217, v217 quad_perm:[2,3,0,1] row_mask:0xf bank_mask:0xf
	v_add_f32_dpp v218, v218, v218 quad_perm:[2,3,0,1] row_mask:0xf bank_mask:0xf
	v_add_f32_dpp v219, v219, v219 quad_perm:[2,3,0,1] row_mask:0xf bank_mask:0xf
	v_add_f32_dpp v220, v220, v220 quad_perm:[2,3,0,1] row_mask:0xf bank_mask:0xf
	v_add_f32_dpp v221, v221, v221 quad_perm:[2,3,0,1] row_mask:0xf bank_mask:0xf
	v_add_f32_dpp v222, v222, v222 quad_perm:[2,3,0,1] row_mask:0xf bank_mask:0xf
	v_add_f32_dpp v223, v223, v223 quad_perm:[2,3,0,1] row_mask:0xf bank_mask:0xf
	v_add_f32_dpp v224, v224, v224 quad_perm:[2,3,0,1] row_mask:0xf bank_mask:0xf
	v_add_f32_dpp v225, v225, v225 quad_perm:[2,3,0,1] row_mask:0xf bank_mask:0xf
	v_add_f32_dpp v226, v226, v226 quad_perm:[2,3,0,1] row_mask:0xf bank_mask:0xf
	v_add_f32_dpp v227, v227, v227 quad_perm:[2,3,0,1] row_mask:0xf bank_mask:0xf
	v_add_f32_dpp v228, v228, v228 quad_perm:[2,3,0,1] row_mask:0xf bank_mask:0xf
	v_add_f32_dpp v229, v229, v229 quad_perm:[2,3,0,1] row_mask:0xf bank_mask:0xf
	v_add_f32_dpp v230, v230, v230 quad_perm:[2,3,0,1] row_mask:0xf bank_mask:0xf
	v_add_f32_dpp v231, v231, v231 quad_perm:[2,3,0,1] row_mask:0xf bank_mask:0xf
	v_add_f32_dpp v232, v232, v232 quad_perm:[2,3,0,1] row_mask:0xf bank_mask:0xf
	v_add_f32_dpp v233, v233, v233 quad_perm:[2,3,0,1] row_mask:0xf bank_mask:0xf
	v_add_f32_dpp v234, v234, v234 quad_perm:[2,3,0,1] row_mask:0xf bank_mask:0xf
	v_add_f32_dpp v235, v235, v235 quad_perm:[2,3,0,1] row_mask:0xf bank_mask:0xf
	v_add_f32_dpp v204, v204, v204 row_half_mirror row_mask:0xf bank_mask:0xf
	v_add_f32_dpp v205, v205, v205 row_half_mirror row_mask:0xf bank_mask:0xf
	v_add_f32_dpp v206, v206, v206 row_half_mirror row_mask:0xf bank_mask:0xf
	v_add_f32_dpp v207, v207, v207 row_half_mirror row_mask:0xf bank_mask:0xf
	v_add_f32_dpp v208, v208, v208 row_half_mirror row_mask:0xf bank_mask:0xf
	v_add_f32_dpp v209, v209, v209 row_half_mirror row_mask:0xf bank_mask:0xf
	v_add_f32_dpp v210, v210, v210 row_half_mirror row_mask:0xf bank_mask:0xf
	v_add_f32_dpp v211, v211, v211 row_half_mirror row_mask:0xf bank_mask:0xf
	v_add_f32_dpp v212, v212, v212 row_half_mirror row_mask:0xf bank_mask:0xf
	v_add_f32_dpp v213, v213, v213 row_half_mirror row_mask:0xf bank_mask:0xf
	v_add_f32_dpp v214, v214, v214 row_half_mirror row_mask:0xf bank_mask:0xf
	v_add_f32_dpp v215, v215, v215 row_half_mirror row_mask:0xf bank_mask:0xf
	v_add_f32_dpp v216, v216, v216 row_half_mirror row_mask:0xf bank_mask:0xf
	v_add_f32_dpp v217, v217, v217 row_half_mirror row_mask:0xf bank_mask:0xf
	v_add_f32_dpp v218, v218, v218 row_half_mirror row_mask:0xf bank_mask:0xf
	v_add_f32_dpp v219, v219, v219 row_half_mirror row_mask:0xf bank_mask:0xf
	v_add_f32_dpp v220, v220, v220 row_half_mirror row_mask:0xf bank_mask:0xf
	v_add_f32_dpp v221, v221, v221 row_half_mirror row_mask:0xf bank_mask:0xf
	v_add_f32_dpp v222, v222, v222 row_half_mirror row_mask:0xf bank_mask:0xf
	v_add_f32_dpp v223, v223, v223 row_half_mirror row_mask:0xf bank_mask:0xf
	v_add_f32_dpp v224, v224, v224 row_half_mirror row_mask:0xf bank_mask:0xf
	v_add_f32_dpp v225, v225, v225 row_half_mirror row_mask:0xf bank_mask:0xf
	v_add_f32_dpp v226, v226, v226 row_half_mirror row_mask:0xf bank_mask:0xf
	v_add_f32_dpp v227, v227, v227 row_half_mirror row_mask:0xf bank_mask:0xf
	v_add_f32_dpp v228, v228, v228 row_half_mirror row_mask:0xf bank_mask:0xf
	v_add_f32_dpp v229, v229, v229 row_half_mirror row_mask:0xf bank_mask:0xf
	v_add_f32_dpp v230, v230, v230 row_half_mirror row_mask:0xf bank_mask:0xf
	v_add_f32_dpp v231, v231, v231 row_half_mirror row_mask:0xf bank_mask:0xf
	v_add_f32_dpp v232, v232, v232 row_half_mirror row_mask:0xf bank_mask:0xf
	v_add_f32_dpp v233, v233, v233 row_half_mirror row_mask:0xf bank_mask:0xf
	v_add_f32_dpp v234, v234, v234 row_half_mirror row_mask:0xf bank_mask:0xf
	v_add_f32_dpp v235, v235, v235 row_half_mirror row_mask:0xf bank_mask:0xf
	v_add_f32_dpp v204, v204, v204 row_mirror row_mask:0xf bank_mask:0xf
	v_add_f32_dpp v205, v205, v205 row_mirror row_mask:0xf bank_mask:0xf
	v_add_f32_dpp v206, v206, v206 row_mirror row_mask:0xf bank_mask:0xf
	v_add_f32_dpp v207, v207, v207 row_mirror row_mask:0xf bank_mask:0xf
	v_add_f32_dpp v208, v208, v208 row_mirror row_mask:0xf bank_mask:0xf
	v_add_f32_dpp v209, v209, v209 row_mirror row_mask:0xf bank_mask:0xf
	v_add_f32_dpp v210, v210, v210 row_mirror row_mask:0xf bank_mask:0xf
	v_add_f32_dpp v211, v211, v211 row_mirror row_mask:0xf bank_mask:0xf
	v_add_f32_dpp v212, v212, v212 row_mirror row_mask:0xf bank_mask:0xf
	v_add_f32_dpp v213, v213, v213 row_mirror row_mask:0xf bank_mask:0xf
	v_add_f32_dpp v214, v214, v214 row_mirror row_mask:0xf bank_mask:0xf
	v_add_f32_dpp v215, v215, v215 row_mirror row_mask:0xf bank_mask:0xf
	v_add_f32_dpp v216, v216, v216 row_mirror row_mask:0xf bank_mask:0xf
	v_add_f32_dpp v217, v217, v217 row_mirror row_mask:0xf bank_mask:0xf
	v_add_f32_dpp v218, v218, v218 row_mirror row_mask:0xf bank_mask:0xf
	v_add_f32_dpp v219, v219, v219 row_mirror row_mask:0xf bank_mask:0xf
	v_add_f32_dpp v220, v220, v220 row_mirror row_mask:0xf bank_mask:0xf
	v_add_f32_dpp v221, v221, v221 row_mirror row_mask:0xf bank_mask:0xf
	v_add_f32_dpp v222, v222, v222 row_mirror row_mask:0xf bank_mask:0xf
	v_add_f32_dpp v223, v223, v223 row_mirror row_mask:0xf bank_mask:0xf
	v_add_f32_dpp v224, v224, v224 row_mirror row_mask:0xf bank_mask:0xf
	v_add_f32_dpp v225, v225, v225 row_mirror row_mask:0xf bank_mask:0xf
	v_add_f32_dpp v226, v226, v226 row_mirror row_mask:0xf bank_mask:0xf
	v_add_f32_dpp v227, v227, v227 row_mirror row_mask:0xf bank_mask:0xf
	v_add_f32_dpp v228, v228, v228 row_mirror row_mask:0xf bank_mask:0xf
	v_add_f32_dpp v229, v229, v229 row_mirror row_mask:0xf bank_mask:0xf
	v_add_f32_dpp v230, v230, v230 row_mirror row_mask:0xf bank_mask:0xf
	v_add_f32_dpp v231, v231, v231 row_mirror row_mask:0xf bank_mask:0xf
	v_add_f32_dpp v232, v232, v232 row_mirror row_mask:0xf bank_mask:0xf
	v_add_f32_dpp v233, v233, v233 row_mirror row_mask:0xf bank_mask:0xf
	v_add_f32_dpp v234, v234, v234 row_mirror row_mask:0xf bank_mask:0xf
	v_add_f32_dpp v235, v235, v235 row_mirror row_mask:0xf bank_mask:0xf
	v_add_f32_dpp v204, v204, v204 row_bcast:15 row_mask:0xa bank_mask:0xf
	v_add_f32_dpp v205, v205, v205 row_bcast:15 row_mask:0xa bank_mask:0xf
	v_add_f32_dpp v206, v206, v206 row_bcast:15 row_mask:0xa bank_mask:0xf
	v_add_f32_dpp v207, v207, v207 row_bcast:15 row_mask:0xa bank_mask:0xf
	v_add_f32_dpp v208, v208, v208 row_bcast:15 row_mask:0xa bank_mask:0xf
	v_add_f32_dpp v209, v209, v209 row_bcast:15 row_mask:0xa bank_mask:0xf
	v_add_f32_dpp v210, v210, v210 row_bcast:15 row_mask:0xa bank_mask:0xf
	v_add_f32_dpp v211, v211, v211 row_bcast:15 row_mask:0xa bank_mask:0xf
	v_add_f32_dpp v212, v212, v212 row_bcast:15 row_mask:0xa bank_mask:0xf
	v_add_f32_dpp v213, v213, v213 row_bcast:15 row_mask:0xa bank_mask:0xf
	v_add_f32_dpp v214, v214, v214 row_bcast:15 row_mask:0xa bank_mask:0xf
	v_add_f32_dpp v215, v215, v215 row_bcast:15 row_mask:0xa bank_mask:0xf
	v_add_f32_dpp v216, v216, v216 row_bcast:15 row_mask:0xa bank_mask:0xf
	v_add_f32_dpp v217, v217, v217 row_bcast:15 row_mask:0xa bank_mask:0xf
	v_add_f32_dpp v218, v218, v218 row_bcast:15 row_mask:0xa bank_mask:0xf
	v_add_f32_dpp v219, v219, v219 row_bcast:15 row_mask:0xa bank_mask:0xf
	v_add_f32_dpp v220, v220, v220 row_bcast:15 row_mask:0xa bank_mask:0xf
	v_add_f32_dpp v221, v221, v221 row_bcast:15 row_mask:0xa bank_mask:0xf
	v_add_f32_dpp v222, v222, v222 row_bcast:15 row_mask:0xa bank_mask:0xf
	v_add_f32_dpp v223, v223, v223 row_bcast:15 row_mask:0xa bank_mask:0xf
	v_add_f32_dpp v224, v224, v224 row_bcast:15 row_mask:0xa bank_mask:0xf
	v_add_f32_dpp v225, v225, v225 row_bcast:15 row_mask:0xa bank_mask:0xf
	v_add_f32_dpp v226, v226, v226 row_bcast:15 row_mask:0xa bank_mask:0xf
	v_add_f32_dpp v227, v227, v227 row_bcast:15 row_mask:0xa bank_mask:0xf
	v_add_f32_dpp v228, v228, v228 row_bcast:15 row_mask:0xa bank_mask:0xf
	v_add_f32_dpp v229, v229, v229 row_bcast:15 row_mask:0xa bank_mask:0xf
	v_add_f32_dpp v230, v230, v230 row_bcast:15 row_mask:0xa bank_mask:0xf
	v_add_f32_dpp v231, v231, v231 row_bcast:15 row_mask:0xa bank_mask:0xf
	v_add_f32_dpp v232, v232, v232 row_bcast:15 row_mask:0xa bank_mask:0xf
	v_add_f32_dpp v233, v233, v233 row_bcast:15 row_mask:0xa bank_mask:0xf
	v_add_f32_dpp v234, v234, v234 row_bcast:15 row_mask:0xa bank_mask:0xf
	v_add_f32_dpp v235, v235, v235 row_bcast:15 row_mask:0xa bank_mask:0xf
	v_add_f32_dpp v204, v204, v204 row_bcast:31 row_mask:0xc bank_mask:0xf
	v_add_f32_dpp v205, v205, v205 row_bcast:31 row_mask:0xc bank_mask:0xf
	v_add_f32_dpp v206, v206, v206 row_bcast:31 row_mask:0xc bank_mask:0xf
	v_add_f32_dpp v207, v207, v207 row_bcast:31 row_mask:0xc bank_mask:0xf
	v_add_f32_dpp v208, v208, v208 row_bcast:31 row_mask:0xc bank_mask:0xf
	v_add_f32_dpp v209, v209, v209 row_bcast:31 row_mask:0xc bank_mask:0xf
	v_add_f32_dpp v210, v210, v210 row_bcast:31 row_mask:0xc bank_mask:0xf
	v_add_f32_dpp v211, v211, v211 row_bcast:31 row_mask:0xc bank_mask:0xf
	v_add_f32_dpp v212, v212, v212 row_bcast:31 row_mask:0xc bank_mask:0xf
	v_add_f32_dpp v213, v213, v213 row_bcast:31 row_mask:0xc bank_mask:0xf
	v_add_f32_dpp v214, v214, v214 row_bcast:31 row_mask:0xc bank_mask:0xf
	v_add_f32_dpp v215, v215, v215 row_bcast:31 row_mask:0xc bank_mask:0xf
	v_add_f32_dpp v216, v216, v216 row_bcast:31 row_mask:0xc bank_mask:0xf
	v_add_f32_dpp v217, v217, v217 row_bcast:31 row_mask:0xc bank_mask:0xf
	v_add_f32_dpp v218, v218, v218 row_bcast:31 row_mask:0xc bank_mask:0xf
	v_add_f32_dpp v219, v219, v219 row_bcast:31 row_mask:0xc bank_mask:0xf
	v_add_f32_dpp v220, v220, v220 row_bcast:31 row_mask:0xc bank_mask:0xf
	v_add_f32_dpp v221, v221, v221 row_bcast:31 row_mask:0xc bank_mask:0xf
	v_add_f32_dpp v222, v222, v222 row_bcast:31 row_mask:0xc bank_mask:0xf
	v_add_f32_dpp v223, v223, v223 row_bcast:31 row_mask:0xc bank_mask:0xf
	v_add_f32_dpp v224, v224, v224 row_bcast:31 row_mask:0xc bank_mask:0xf
	v_add_f32_dpp v225, v225, v225 row_bcast:31 row_mask:0xc bank_mask:0xf
	v_add_f32_dpp v226, v226, v226 row_bcast:31 row_mask:0xc bank_mask:0xf
	v_add_f32_dpp v227, v227, v227 row_bcast:31 row_mask:0xc bank_mask:0xf
	v_add_f32_dpp v228, v228, v228 row_bcast:31 row_mask:0xc bank_mask:0xf
	v_add_f32_dpp v229, v229, v229 row_bcast:31 row_mask:0xc bank_mask:0xf
	v_add_f32_dpp v230, v230, v230 row_bcast:31 row_mask:0xc bank_mask:0xf
	v_add_f32_dpp v231, v231, v231 row_bcast:31 row_mask:0xc bank_mask:0xf
	v_add_f32_dpp v232, v232, v232 row_bcast:31 row_mask:0xc bank_mask:0xf
	v_add_f32_dpp v233, v233, v233 row_bcast:31 row_mask:0xc bank_mask:0xf
	v_add_f32_dpp v234, v234, v234 row_bcast:31 row_mask:0xc bank_mask:0xf
	v_add_f32_dpp v235, v235, v235 row_bcast:31 row_mask:0xc bank_mask:0xf
	v_cmp_eq_u32_e32 vcc, 0xfc0, v1
	s_and_saveexec_b64 s[24:25], vcc
	s_waitcnt lgkmcnt(0)
	v_add_f32_e32 v204, s16, v204
	v_add_f32_e32 v205, s17, v205
	v_add_f32_e32 v206, s18, v206
	v_add_f32_e32 v207, s19, v207
	v_add_f32_e32 v208, s20, v208
	v_add_f32_e32 v209, s21, v209
	v_add_f32_e32 v210, s22, v210
	v_add_f32_e32 v211, s23, v211
	v_add_f32_e32 v212, s16, v212
	v_add_f32_e32 v213, s17, v213
	v_add_f32_e32 v214, s18, v214
	v_add_f32_e32 v215, s19, v215
	v_add_f32_e32 v216, s20, v216
	v_add_f32_e32 v217, s21, v217
	v_add_f32_e32 v218, s22, v218
	v_add_f32_e32 v219, s23, v219
	v_add_f32_e32 v220, s16, v220
	v_add_f32_e32 v221, s17, v221
	v_add_f32_e32 v222, s18, v222
	v_add_f32_e32 v223, s19, v223
	v_add_f32_e32 v224, s20, v224
	v_add_f32_e32 v225, s21, v225
	v_add_f32_e32 v226, s22, v226
	v_add_f32_e32 v227, s23, v227
	v_add_f32_e32 v228, s16, v228
	v_add_f32_e32 v229, s17, v229
	v_add_f32_e32 v230, s18, v230
	v_add_f32_e32 v231, s19, v231
	v_add_f32_e32 v232, s20, v232
	v_add_f32_e32 v233, s21, v233
	v_add_f32_e32 v234, s22, v234
	v_add_f32_e32 v235, s23, v235
	v_mul_f32_e32 v204, 0x4038aa3b, v204
	v_mul_f32_e32 v205, 0x4038aa3b, v205
	v_mul_f32_e32 v206, 0x4038aa3b, v206
	v_mul_f32_e32 v207, 0x4038aa3b, v207
	v_mul_f32_e32 v208, 0x4038aa3b, v208
	v_mul_f32_e32 v209, 0x4038aa3b, v209
	v_mul_f32_e32 v210, 0x4038aa3b, v210
	v_mul_f32_e32 v211, 0x4038aa3b, v211
	v_mul_f32_e32 v212, 0x4038aa3b, v212
	v_mul_f32_e32 v213, 0x4038aa3b, v213
	v_mul_f32_e32 v214, 0x4038aa3b, v214
	v_mul_f32_e32 v215, 0x4038aa3b, v215
	v_mul_f32_e32 v216, 0x4038aa3b, v216
	v_mul_f32_e32 v217, 0x4038aa3b, v217
	v_mul_f32_e32 v218, 0x4038aa3b, v218
	v_mul_f32_e32 v219, 0x4038aa3b, v219
	v_mul_f32_e32 v220, 0x4038aa3b, v220
	v_mul_f32_e32 v221, 0x4038aa3b, v221
	v_mul_f32_e32 v222, 0x4038aa3b, v222
	v_mul_f32_e32 v223, 0x4038aa3b, v223
	v_mul_f32_e32 v224, 0x4038aa3b, v224
	v_mul_f32_e32 v225, 0x4038aa3b, v225
	v_mul_f32_e32 v226, 0x4038aa3b, v226
	v_mul_f32_e32 v227, 0x4038aa3b, v227
	v_mul_f32_e32 v228, 0x4038aa3b, v228
	v_mul_f32_e32 v229, 0x4038aa3b, v229
	v_mul_f32_e32 v230, 0x4038aa3b, v230
	v_mul_f32_e32 v231, 0x4038aa3b, v231
	v_mul_f32_e32 v232, 0x4038aa3b, v232
	v_mul_f32_e32 v233, 0x4038aa3b, v233
	v_mul_f32_e32 v234, 0x4038aa3b, v234
	v_mul_f32_e32 v235, 0x4038aa3b, v235
	global_store_dwordx4 v10, v[204:207], s[14:15]
	global_store_dwordx4 v10, v[208:211], s[14:15] offset:16
	v_add_u32_e32 v9, 0x1000, v10
	global_store_dwordx4 v9, v[212:215], s[14:15]
	global_store_dwordx4 v9, v[216:219], s[14:15] offset:16
	v_add_u32_e32 v8, 0x2000, v10
	global_store_dwordx4 v8, v[220:223], s[14:15]
	global_store_dwordx4 v8, v[224:227], s[14:15] offset:16
	v_add_u32_e32 v9, 0x3000, v10
	global_store_dwordx4 v9, v[228:231], s[14:15]
	global_store_dwordx4 v9, v[232:235], s[14:15] offset:16
	s_endpgm

	.amdhsa_kernel _Z11prep_kernelPKfS0_S0_S0_S0_PDF16_S1_Pf
		.amdhsa_group_segment_fixed_size 0
		.amdhsa_private_segment_fixed_size 0
		.amdhsa_kernarg_size 64
		.amdhsa_user_sgpr_count 2
		.amdhsa_user_sgpr_dispatch_ptr 0
		.amdhsa_user_sgpr_queue_ptr 0
		.amdhsa_user_sgpr_kernarg_segment_ptr 1
		.amdhsa_user_sgpr_dispatch_id 0
		.amdhsa_user_sgpr_kernarg_preload_length 0
		.amdhsa_user_sgpr_kernarg_preload_offset 0
		.amdhsa_user_sgpr_private_segment_size 0
		.amdhsa_uses_dynamic_stack 0
		.amdhsa_enable_private_segment 0
		.amdhsa_system_sgpr_workgroup_id_x 1
		.amdhsa_system_sgpr_workgroup_id_y 0
		.amdhsa_system_sgpr_workgroup_id_z 0
		.amdhsa_system_sgpr_workgroup_info 0
		.amdhsa_system_vgpr_workitem_id 0
		.amdhsa_next_free_vgpr 236
		.amdhsa_next_free_sgpr 28
		.amdhsa_accum_offset 236
		.amdhsa_reserve_vcc 1
		.amdhsa_float_round_mode_32 0
		.amdhsa_float_round_mode_16_64 0
		.amdhsa_float_denorm_mode_32 3
		.amdhsa_float_denorm_mode_16_64 3
		.amdhsa_dx10_clamp 1
		.amdhsa_ieee_mode 1
		.amdhsa_fp16_overflow 0
		.amdhsa_tg_split 0
		.amdhsa_exception_fp_ieee_invalid_op 0
		.amdhsa_exception_fp_denorm_src 0
		.amdhsa_exception_fp_ieee_div_zero 0
		.amdhsa_exception_fp_ieee_overflow 0
		.amdhsa_exception_fp_ieee_underflow 0
		.amdhsa_exception_fp_ieee_inexact 0
		.amdhsa_exception_int_div_zero 0
	.end_amdhsa_kernel

amdhsa.kernels:
  - .agpr_count:     0
    .args:
      - .actual_access:  read_only
        .address_space:  global
        .offset:         0
        .size:           8
        .value_kind:     global_buffer
      - .actual_access:  read_only
        .address_space:  global
        .offset:         8
        .size:           8
        .value_kind:     global_buffer
      - .actual_access:  read_only
        .address_space:  global
        .offset:         16
        .size:           8
        .value_kind:     global_buffer
      - .actual_access:  read_only
        .address_space:  global
        .offset:         24
        .size:           8
        .value_kind:     global_buffer
      - .actual_access:  read_only
        .address_space:  global
        .offset:         32
        .size:           8
        .value_kind:     global_buffer
      - .actual_access:  write_only
        .address_space:  global
        .offset:         40
        .size:           8
        .value_kind:     global_buffer
      - .actual_access:  write_only
        .address_space:  global
        .offset:         48
        .size:           8
        .value_kind:     global_buffer
      - .actual_access:  write_only
        .address_space:  global
        .offset:         56
        .size:           8
        .value_kind:     global_buffer
    .group_segment_fixed_size: 0
    .kernarg_segment_align: 8
    .kernarg_segment_size: 64
    .language:       OpenCL C
    .language_version:
      - 2
      - 0
    .max_flat_workgroup_size: 256
    .name:           _Z11prep_kernelPKfS0_S0_S0_S0_PDF16_S1_Pf
    .private_segment_fixed_size: 0
    .sgpr_count:     34
    .sgpr_spill_count: 0
    .symbol:         _Z11prep_kernelPKfS0_S0_S0_S0_PDF16_S1_Pf.kd
    .uniform_work_group_size: 1
    .uses_dynamic_stack: false
    .vgpr_count:     236
    .vgpr_spill_count: 0
    .wavefront_size: 64
  - .agpr_count:     0
    .args:
      - .address_space:  global
        .offset:         0
        .size:           8
        .value_kind:     global_buffer
      - .address_space:  global
        .offset:         8
        .size:           8
        .value_kind:     global_buffer
      - .actual_access:  read_only
        .address_space:  global
        .offset:         16
        .size:           8
        .value_kind:     global_buffer
      - .address_space:  global
        .offset:         24
        .size:           8
        .value_kind:     global_buffer
      - .actual_access:  read_only
        .address_space:  global
        .offset:         32
        .size:           8
        .value_kind:     global_buffer
      - .actual_access:  read_only
        .address_space:  global
        .offset:         40
        .size:           8
        .value_kind:     global_buffer
      - .actual_access:  read_only
        .address_space:  global
        .offset:         48
        .size:           8
        .value_kind:     global_buffer
      - .actual_access:  write_only
        .address_space:  global
        .offset:         56
        .size:           8
        .value_kind:     global_buffer
      - .actual_access:  write_only
        .address_space:  global
        .offset:         64
        .size:           8
        .value_kind:     global_buffer
    .group_segment_fixed_size: 163840
    .kernarg_segment_align: 8
    .kernarg_segment_size: 72
    .language:       OpenCL C
    .language_version:
      - 2
      - 0
    .max_flat_workgroup_size: 512
    .name:           _Z11main_kernelPKDF16_PKfPKiS0_S2_S2_S2_PfS5_
    .private_segment_fixed_size: 0
    .sgpr_count:     108
    .sgpr_spill_count: 0
    .symbol:         _Z11main_kernelPKDF16_PKfPKiS0_S2_S2_S2_PfS5_.kd
    .uniform_work_group_size: 1
    .uses_dynamic_stack: false
    .vgpr_count:     256
    .vgpr_spill_count: 0
    .wavefront_size: 64
  - .agpr_count:     0
    .args:
      - .actual_access:  read_only
        .address_space:  global
        .offset:         0
        .size:           8
        .value_kind:     global_buffer
      - .actual_access:  read_only
        .address_space:  global
        .offset:         8
        .size:           8
        .value_kind:     global_buffer
      - .actual_access:  write_only
        .address_space:  global
        .offset:         16
        .size:           8
        .value_kind:     global_buffer
    .group_segment_fixed_size: 32
    .kernarg_segment_align: 8
    .kernarg_segment_size: 24
    .language:       OpenCL C
    .language_version:
      - 2
      - 0
    .max_flat_workgroup_size: 256
    .name:           _Z14combine_kernelPKfS0_Pf
    .private_segment_fixed_size: 0
    .sgpr_count:     26
    .sgpr_spill_count: 0
    .symbol:         _Z14combine_kernelPKfS0_Pf.kd
    .uniform_work_group_size: 1
    .uses_dynamic_stack: false
    .vgpr_count:     40
    .vgpr_spill_count: 0
    .wavefront_size: 64
